# baseline (speedup 1.0000x reference)
.LBB4_20:
	s_or_b64 exec, exec, s[2:3]
	v_lshlrev_b32_e32 v1, 5, v136
	v_or3_b32 v133, v1, v135, s13
	v_lshlrev_b32_e32 v1, 7, v136
	v_lshlrev_b32_e32 v130, 2, v135
	v_add3_u32 v1, s20, v1, v130
	v_add_u32_e32 v137, 0x800, v1
	v_lshlrev_b32_e32 v131, 2, v134
	ds_read2_b32 v[134:135], v137 offset1:16
	s_ashr_i32 s13, s12, 31
	s_lshl_b64 s[0:1], s[12:13], 23
	v_and_b32_e32 v130, 16, v0
	s_add_u32 s0, s14, s0
	s_waitcnt lgkmcnt(0)
	v_mul_f32_e32 v134, 0x3cb17218, v134
	v_pk_mul_f32 v[104:105], v[134:135], v[104:105] op_sel_hi:[0,1]
	v_pk_mul_f32 v[102:103], v[134:135], v[102:103] op_sel_hi:[0,1]
	v_pk_mul_f32 v[98:99], v[134:135], v[98:99] op_sel_hi:[0,1]
	v_cvt_pk_f16_f32 v102, v102, v103
	v_cvt_pk_f16_f32 v103, v104, v105
	v_cvt_pk_f16_f32 v104, v98, v99
	v_mul_f32_e32 v98, 0x3cb17218, v135
	v_pk_mul_f32 v[72:73], v[98:99], v[72:73] op_sel_hi:[0,1]
	v_pk_mul_f32 v[70:71], v[98:99], v[70:71] op_sel_hi:[0,1]
	v_pk_mul_f32 v[66:67], v[98:99], v[66:67] op_sel_hi:[0,1]
	v_cvt_pk_f16_f32 v70, v70, v71
	v_cvt_pk_f16_f32 v71, v72, v73
	v_cvt_pk_f16_f32 v72, v66, v67
	ds_read2_b32 v[66:67], v137 offset0:128 offset1:144
	v_lshlrev_b32_e32 v0, 6, v0
	v_and_or_b32 v136, v131, 8, v130
	s_addc_u32 s1, s15, s1
	v_and_b32_e32 v0, 64, v0
	v_mov_b32_e32 v1, 0
	v_lshl_add_u64 v[130:131], s[0:1], 0, v[0:1]
	v_lshlrev_b32_e32 v0, 1, v136
	v_lshl_add_u64 v[130:131], v[130:131], 0, v[0:1]
	v_lshlrev_b32_e32 v0, 11, v133
	v_and_b32_e32 v0, 0x7b7000, v0
	s_waitcnt lgkmcnt(0)
	v_mul_f32_e32 v66, 0x3cb17218, v66
	v_lshl_add_u64 v[130:131], v[130:131], 0, v[0:1]
	v_pk_mul_f32 v[100:101], v[134:135], v[100:101] op_sel_hi:[0,1]
	s_mov_b64 s[0:1], 0x8000
	v_pk_mul_f32 v[48:49], v[66:67], v[48:49] op_sel_hi:[0,1]
	v_pk_mul_f32 v[46:47], v[66:67], v[46:47] op_sel_hi:[0,1]
	v_pk_mul_f32 v[38:39], v[66:67], v[38:39] op_sel_hi:[0,1]
	v_pk_mul_f32 v[28:29], v[66:67], v[28:29] op_sel_hi:[0,1]
	v_pk_mul_f32 v[26:27], v[66:67], v[26:27] op_sel_hi:[0,1]
	v_lshlrev_b32_e32 v0, 8, v132
	v_cvt_pk_f16_f32 v105, v100, v101
	v_lshl_add_u64 v[100:101], v[130:131], 0, s[0:1]
	v_pk_mul_f32 v[68:69], v[98:99], v[68:69] op_sel_hi:[0,1]
	s_mov_b64 s[0:1], 0x40000
	v_cvt_pk_f16_f32 v46, v46, v47
	v_cvt_pk_f16_f32 v47, v48, v49
	v_cvt_pk_f16_f32 v48, v38, v39
	v_cvt_pk_f16_f32 v26, v26, v27
	v_cvt_pk_f16_f32 v27, v28, v29
	v_pk_mul_f32 v[38:39], v[66:67], v[44:45] op_sel_hi:[0,1]
	v_pk_mul_f32 v[28:29], v[66:67], v[42:43] op_sel_hi:[0,1]
	v_lshl_or_b32 v0, s21, 2, v0
	v_cvt_pk_f16_f32 v73, v68, v69
	v_lshl_add_u64 v[68:69], v[130:131], 0, s[0:1]
	v_pk_mul_f32 v[64:65], v[66:67], v[64:65] op_sel_hi:[0,1]
	v_pk_mul_f32 v[62:63], v[66:67], v[62:63] op_sel_hi:[0,1]
	v_pk_mul_f32 v[58:59], v[66:67], v[58:59] op_sel_hi:[0,1]
	v_cvt_pk_f16_f32 v28, v28, v29
	v_cvt_pk_f16_f32 v29, v38, v39
	v_cvt_pk_f16_f32 v62, v62, v63
	v_cvt_pk_f16_f32 v63, v64, v65
	v_cvt_pk_f16_f32 v64, v58, v59
	v_lshl_add_u64 v[58:59], v[68:69], 0, v[0:1]
	v_pk_mul_f32 v[40:41], v[66:67], v[40:41] op_sel_hi:[0,1]
	v_permlane16_swap_b32_e32 v26, v28
	v_permlane16_swap_b32_e32 v27, v29
	v_mul_f32_e32 v38, 0x3cb17218, v67
	s_mov_b64 s[0:1], 0x48000
	v_pk_mul_f32 v[128:129], v[134:135], v[128:129] op_sel_hi:[0,1]
	v_pk_mul_f32 v[126:127], v[134:135], v[126:127] op_sel_hi:[0,1]
	v_pk_mul_f32 v[122:123], v[134:135], v[122:123] op_sel_hi:[0,1]
	v_pk_mul_f32 v[96:97], v[98:99], v[96:97] op_sel_hi:[0,1]
	v_pk_mul_f32 v[94:95], v[98:99], v[94:95] op_sel_hi:[0,1]
	v_pk_mul_f32 v[90:91], v[98:99], v[90:91] op_sel_hi:[0,1]
	v_pk_mul_f32 v[88:89], v[98:99], v[88:89] op_sel_hi:[0,1]
	v_pk_mul_f32 v[86:87], v[98:99], v[86:87] op_sel_hi:[0,1]
	v_pk_mul_f32 v[82:83], v[98:99], v[82:83] op_sel_hi:[0,1]
	v_cvt_pk_f16_f32 v49, v40, v41
	global_store_dwordx4 v[58:59], v[26:29], off offset:640 nt
	v_lshl_add_u64 v[40:41], v[130:131], 0, s[0:1]
	v_cvt_pk_f16_f32 v126, v126, v127
	v_pk_mul_f32 v[28:29], v[38:39], v[36:37] op_sel_hi:[0,1]
	v_pk_mul_f32 v[26:27], v[38:39], v[34:35] op_sel_hi:[0,1]
	v_cvt_pk_f16_f32 v127, v128, v129
	v_cvt_pk_f16_f32 v128, v122, v123
	v_lshl_add_u64 v[122:123], v[130:131], 0, v[0:1]
	v_cvt_pk_f16_f32 v94, v94, v95
	v_cvt_pk_f16_f32 v95, v96, v97
	v_cvt_pk_f16_f32 v96, v90, v91
	v_lshl_add_u64 v[90:91], v[100:101], 0, v[0:1]
	v_cvt_pk_f16_f32 v86, v86, v87
	v_cvt_pk_f16_f32 v87, v88, v89
	v_cvt_pk_f16_f32 v88, v82, v83
	v_or_b32_e32 v82, 0x80, v0
	v_mov_b32_e32 v83, v1
	v_cvt_pk_f16_f32 v26, v26, v27
	v_cvt_pk_f16_f32 v27, v28, v29
	v_pk_mul_f32 v[28:29], v[38:39], v[30:31] op_sel_hi:[0,1]
	v_lshl_add_u64 v[30:31], v[40:41], 0, v[0:1]
	v_pk_mul_f32 v[0:1], v[38:39], v[24:25] op_sel_hi:[0,1]
	v_pk_mul_f32 v[22:23], v[38:39], v[22:23] op_sel_hi:[0,1]
	v_cvt_pk_f16_f32 v22, v22, v23
	v_cvt_pk_f16_f32 v23, v0, v1
	v_pk_mul_f32 v[0:1], v[38:39], v[20:21] op_sel_hi:[0,1]
	v_pk_mul_f32 v[18:19], v[38:39], v[18:19] op_sel_hi:[0,1]
	v_cvt_pk_f16_f32 v24, v18, v19
	v_cvt_pk_f16_f32 v25, v0, v1
	s_nop 0
	v_permlane16_swap_b32_e32 v22, v24
	v_permlane16_swap_b32_e32 v23, v25
	v_lshl_add_u64 v[0:1], v[40:41], 0, v[82:83]
	global_store_dwordx4 v[0:1], v[22:25], off nt
	v_pk_mul_f32 v[12:13], v[38:39], v[12:13] op_sel_hi:[0,1]
	v_pk_mul_f32 v[0:1], v[38:39], v[10:11] op_sel_hi:[0,1]
	v_pk_mul_f32 v[4:5], v[38:39], v[4:5] op_sel_hi:[0,1]
	v_pk_mul_f32 v[2:3], v[38:39], v[2:3] op_sel_hi:[0,1]
	v_cvt_pk_f16_f32 v0, v0, v1
	v_cvt_pk_f16_f32 v1, v12, v13
	v_cvt_pk_f16_f32 v2, v2, v3
	v_cvt_pk_f16_f32 v3, v4, v5
	s_nop 0
	v_permlane16_swap_b32_e32 v0, v2
	v_permlane16_swap_b32_e32 v1, v3
	global_store_dwordx4 v[30:31], v[0:3], off offset:512 nt
	v_pk_mul_f32 v[124:125], v[134:135], v[124:125] op_sel_hi:[0,1]
	v_pk_mul_f32 v[120:121], v[134:135], v[120:121] op_sel_hi:[0,1]
	v_pk_mul_f32 v[2:3], v[38:39], v[16:17] op_sel_hi:[0,1]
	v_pk_mul_f32 v[0:1], v[38:39], v[14:15] op_sel_hi:[0,1]
	v_pk_mul_f32 v[118:119], v[134:135], v[118:119] op_sel_hi:[0,1]
	v_pk_mul_f32 v[116:117], v[134:135], v[116:117] op_sel_hi:[0,1]
	v_pk_mul_f32 v[114:115], v[134:135], v[114:115] op_sel_hi:[0,1]
	v_pk_mul_f32 v[112:113], v[134:135], v[112:113] op_sel_hi:[0,1]
	v_pk_mul_f32 v[110:111], v[134:135], v[110:111] op_sel_hi:[0,1]
	v_pk_mul_f32 v[108:109], v[134:135], v[108:109] op_sel_hi:[0,1]
	v_pk_mul_f32 v[106:107], v[134:135], v[106:107] op_sel_hi:[0,1]
	v_pk_mul_f32 v[92:93], v[98:99], v[92:93] op_sel_hi:[0,1]
	v_pk_mul_f32 v[84:85], v[98:99], v[84:85] op_sel_hi:[0,1]
	v_pk_mul_f32 v[80:81], v[98:99], v[80:81] op_sel_hi:[0,1]
	v_pk_mul_f32 v[78:79], v[98:99], v[78:79] op_sel_hi:[0,1]
	v_pk_mul_f32 v[76:77], v[98:99], v[76:77] op_sel_hi:[0,1]
	v_pk_mul_f32 v[74:75], v[98:99], v[74:75] op_sel_hi:[0,1]
	v_pk_mul_f32 v[60:61], v[66:67], v[60:61] op_sel_hi:[0,1]
	v_pk_mul_f32 v[56:57], v[66:67], v[56:57] op_sel_hi:[0,1]
	v_pk_mul_f32 v[54:55], v[66:67], v[54:55] op_sel_hi:[0,1]
	v_pk_mul_f32 v[52:53], v[66:67], v[52:53] op_sel_hi:[0,1]
	v_pk_mul_f32 v[50:51], v[66:67], v[50:51] op_sel_hi:[0,1]
	v_pk_mul_f32 v[32:33], v[38:39], v[32:33] op_sel_hi:[0,1]
	v_cvt_pk_f16_f32 v0, v0, v1
	v_cvt_pk_f16_f32 v1, v2, v3
	v_pk_mul_f32 v[4:5], v[38:39], v[8:9] op_sel_hi:[0,1]
	v_pk_mul_f32 v[2:3], v[38:39], v[6:7] op_sel_hi:[0,1]
	v_cvt_pk_f16_f32 v129, v124, v125
	v_cvt_pk_f16_f32 v118, v118, v119
	v_cvt_pk_f16_f32 v119, v120, v121
	v_cvt_pk_f16_f32 v120, v114, v115
	v_cvt_pk_f16_f32 v121, v116, v117
	v_cvt_pk_f16_f32 v110, v110, v111
	v_cvt_pk_f16_f32 v111, v112, v113
	v_cvt_pk_f16_f32 v112, v106, v107
	v_cvt_pk_f16_f32 v113, v108, v109
	v_cvt_pk_f16_f32 v97, v92, v93
	v_cvt_pk_f16_f32 v89, v84, v85
	v_cvt_pk_f16_f32 v78, v78, v79
	v_cvt_pk_f16_f32 v79, v80, v81
	v_cvt_pk_f16_f32 v80, v74, v75
	v_cvt_pk_f16_f32 v81, v76, v77
	v_cvt_pk_f16_f32 v65, v60, v61
	v_cvt_pk_f16_f32 v54, v54, v55
	v_cvt_pk_f16_f32 v55, v56, v57
	v_cvt_pk_f16_f32 v56, v50, v51
	v_cvt_pk_f16_f32 v57, v52, v53
	v_cvt_pk_f16_f32 v28, v28, v29
	v_cvt_pk_f16_f32 v29, v32, v33
	v_cvt_pk_f16_f32 v2, v2, v3
	v_cvt_pk_f16_f32 v3, v4, v5
	v_permlane16_swap_b32_e32 v126, v128
	v_permlane16_swap_b32_e32 v127, v129
	v_permlane16_swap_b32_e32 v118, v120
	v_permlane16_swap_b32_e32 v119, v121
	v_permlane16_swap_b32_e32 v110, v112
	v_permlane16_swap_b32_e32 v111, v113
	v_permlane16_swap_b32_e32 v102, v104
	v_permlane16_swap_b32_e32 v103, v105
	v_permlane16_swap_b32_e32 v94, v96
	v_permlane16_swap_b32_e32 v95, v97
	v_permlane16_swap_b32_e32 v86, v88
	v_permlane16_swap_b32_e32 v87, v89
	v_lshl_add_u64 v[84:85], v[100:101], 0, v[82:83]
	v_permlane16_swap_b32_e32 v78, v80
	v_permlane16_swap_b32_e32 v79, v81
	v_permlane16_swap_b32_e32 v70, v72
	v_permlane16_swap_b32_e32 v71, v73
	v_permlane16_swap_b32_e32 v62, v64
	v_permlane16_swap_b32_e32 v63, v65
	v_permlane16_swap_b32_e32 v54, v56
	v_permlane16_swap_b32_e32 v55, v57
	v_lshl_add_u64 v[50:51], v[68:69], 0, v[82:83]
	v_permlane16_swap_b32_e32 v46, v48
	v_permlane16_swap_b32_e32 v47, v49
	v_permlane16_swap_b32_e32 v26, v28
	v_permlane16_swap_b32_e32 v27, v29
	v_permlane16_swap_b32_e32 v0, v2
	v_permlane16_swap_b32_e32 v1, v3
	global_store_dwordx4 v[122:123], v[126:129], off nt
	global_store_dwordx4 v[122:123], v[118:121], off offset:128 nt
	global_store_dwordx4 v[122:123], v[110:113], off offset:512 nt
	global_store_dwordx4 v[122:123], v[102:105], off offset:640 nt
	global_store_dwordx4 v[90:91], v[94:97], off nt
	global_store_dwordx4 v[84:85], v[86:89], off nt
	global_store_dwordx4 v[90:91], v[78:81], off offset:512 nt
	global_store_dwordx4 v[90:91], v[70:73], off offset:640 nt
	global_store_dwordx4 v[58:59], v[62:65], off nt
	global_store_dwordx4 v[50:51], v[54:57], off nt
	global_store_dwordx4 v[58:59], v[46:49], off offset:512 nt
	global_store_dwordx4 v[30:31], v[26:29], off nt
	global_store_dwordx4 v[30:31], v[0:3], off offset:640 nt
	s_endpgm
	.p2alignl 8, 3212836864
